# baseline (speedup 1.0000x reference)
.LBB2_70:
	s_and_b64 vcc, exec, s[30:31]
	s_cbranch_vccz .LBB2_112
	v_cmp_gt_u32_e64 s[0:1], 10, v0
	s_mov_b32 s25, 0
	s_nop 0
	v_cndmask_b32_e64 v2, 0, v0, s[0:1]
	v_mad_u64_u32 v[2:3], s[2:3], s24, 10, v[2:3]
	v_mov_b32_e32 v3, 0
	s_waitcnt lgkmcnt(0)
	v_lshl_add_u64 v[4:5], v[2:3], 2, s[14:15]
	global_load_dword v6, v[4:5], off
	s_lshl_b64 s[2:3], s[24:25], 2
	s_add_u32 s2, s16, s2
	s_addc_u32 s3, s17, s3
	s_load_dword s14, s[2:3], 0x0
	s_mul_i32 s2, s24, 0x30000
	s_add_u32 s2, s18, s2
	s_addc_u32 s3, s19, 0
	v_lshlrev_b32_e32 v4, 2, v0
	v_add_u32_e32 v2, 0x2000, v4
	global_load_dword v20, v2, s[2:3] offset:-4096
	global_load_dword v22, v2, s[2:3]
	v_add_u32_e32 v2, 0x4000, v4
	global_load_dword v18, v2, s[2:3] offset:-4096
	global_load_dword v24, v2, s[2:3]
	v_add_u32_e32 v2, 0x6000, v4
	global_load_dword v21, v2, s[2:3] offset:-4096
	global_load_dword v23, v2, s[2:3]
	v_add_u32_e32 v2, 0x8000, v4
	global_load_dword v19, v2, s[2:3] offset:-4096
	global_load_dword v25, v2, s[2:3]
	v_add_u32_e32 v2, 0xa000, v4
	global_load_dword v29, v2, s[2:3] offset:-4096
	v_add_u32_e32 v2, 0xc000, v4
	global_load_dword v5, v2, s[2:3] offset:-4096
	global_load_dword v26, v2, s[2:3]
	v_add_u32_e32 v2, 0xe000, v4
	global_load_dword v31, v2, s[2:3] offset:-4096
	global_load_dword v30, v2, s[2:3]
	v_add_u32_e32 v2, 0x10000, v4
	global_load_dword v34, v2, s[2:3] offset:-4096
	global_load_dword v28, v2, s[2:3]
	v_add_u32_e32 v2, 0x12000, v4
	global_load_dword v35, v2, s[2:3] offset:-4096
	global_load_dword v42, v2, s[2:3]
	v_add_u32_e32 v2, 0x14000, v4
	global_load_dword v46, v2, s[2:3] offset:-4096
	global_load_dword v39, v2, s[2:3]
	v_add_u32_e32 v2, 0x16000, v4
	global_load_dword v45, v2, s[2:3] offset:-4096
	v_add_u32_e32 v2, 0x18000, v4
	global_load_dword v27, v2, s[2:3]
	v_add_u32_e32 v2, 0x1a000, v4
	global_load_dword v33, v2, s[2:3] offset:-4096
	global_load_dword v32, v2, s[2:3]
	v_add_u32_e32 v2, 0x1c000, v4
	global_load_dword v36, v2, s[2:3] offset:-4096
	global_load_dword v47, v4, s[2:3]
	global_load_dword v37, v2, s[2:3]
	v_add_u32_e32 v2, 0x1e000, v4
	global_load_dword v41, v2, s[2:3] offset:-4096
	global_load_dword v40, v2, s[2:3]
	v_add_u32_e32 v2, 0x20000, v4
	global_load_dword v44, v2, s[2:3] offset:-4096
	global_load_dword v38, v2, s[2:3]
	v_add_u32_e32 v2, 0x22000, v4
	global_load_dword v43, v2, s[2:3] offset:-4096
	s_waitcnt lgkmcnt(0)
	s_add_i32 s15, s14, 0x7f
	s_and_b32 s15, s15, 0xffffff80
	v_cmp_gt_i32_e32 vcc, s15, v0
	s_nop 1
	s_mov_b64 s[46:47], vcc
	s_and_saveexec_b64 s[6:7], vcc
	s_cbranch_execz .LBB2_85
	s_cmpk_gt_i32 s14, 0x360
	s_cselect_b64 s[8:9], -1, 0
	s_cmpk_lt_i32 s14, 0x361
	s_cbranch_scc1 .LBB2_74
	v_add_u32_e32 v2, 0x24000, v4
	global_load_dword v7, v2, s[2:3]
	v_add_u32_e32 v2, 0x26000, v4
	global_load_dword v8, v2, s[2:3] offset:-4096
	global_load_dword v9, v2, s[2:3]
	v_add_u32_e32 v2, 0x28000, v4
	global_load_dword v10, v2, s[2:3] offset:-4096
	global_load_dword v11, v2, s[2:3]
	v_add_u32_e32 v2, 0x2a000, v4
	global_load_dword v12, v2, s[2:3] offset:-4096
	global_load_dword v13, v2, s[2:3]
	v_add_u32_e32 v2, 0x2c000, v4
	global_load_dword v14, v2, s[2:3] offset:-4096
	global_load_dword v15, v2, s[2:3]
	v_add_u32_e32 v2, 0x2e000, v4
	global_load_dword v16, v2, s[2:3] offset:-4096
